# baseline (speedup 1.0000x reference)
_Z11gemm_kernelILi128ELi192ELi1EEv8GemmArgs:
	s_load_dwordx2 s[4:5], s[0:1], 0x38
	s_addk_i32 s2, 0xe0
	s_mov_b32 s3, 0
	s_lshl_b64 s[6:7], s[2:3], 2
	s_waitcnt lgkmcnt(0)
	s_add_u32 s4, s4, s6
	s_addc_u32 s5, s5, s7
	s_load_dword s8, s[4:5], 0x0
	s_waitcnt lgkmcnt(0)
	s_cmp_lt_i32 s8, 0
	s_cbranch_scc1 .LBB3_4
	s_load_dwordx2 s[6:7], s[0:1], 0x48
	s_load_dwordx2 s[4:5], s[0:1], 0x0
	v_lshlrev_b32_e32 v64, 4, v0
	v_and_b32_e32 v1, 32, v0
	v_bitop3_b32 v1, v64, v1, 48 bitop3:0x6c
	s_and_b32 s2, s8, 0xffff
	v_bfe_u32 v4, v0, 2, 4
	v_lshrrev_b32_e32 v2, 1, v0
	v_lshrrev_b32_e32 v1, 1, v1
	v_lshrrev_b32_e32 v6, 3, v0
	v_and_or_b32 v1, v2, 32, v1
	v_add_u32_e32 v5, s2, v4
	v_and_b32_e32 v7, 48, v6
	s_movk_i32 s10, 0x70
	v_add_lshl_u32 v22, v5, v7, 12
	v_mov_b32_e32 v23, 0
	v_lshlrev_b32_e32 v44, 1, v1
	v_bitop3_b32 v1, v6, s10, 64 bitop3:0xc8
	s_waitcnt lgkmcnt(0)
	v_lshl_add_u64 v[2:3], s[4:5], 0, v[22:23]
	v_mov_b32_e32 v45, v23
	v_add_lshl_u32 v48, v5, v1, 12
	v_mov_b32_e32 v49, v23
	s_lshr_b32 s10, s8, 24
	s_bfe_u32 s9, s8, 0x80010
	v_lshl_add_u64 v[46:47], v[2:3], 0, v[44:45]
	v_lshl_add_u64 v[2:3], s[4:5], 0, v[48:49]
	s_mulk_i32 s10, 0x300
	v_lshl_add_u64 v[50:51], v[2:3], 0, v[44:45]
	s_mul_i32 s8, s9, 0xc0
	v_or_b32_e32 v2, s10, v4
	v_add_u32_e32 v4, s8, v2
	v_or_b32_e32 v2, v4, v7
	v_lshlrev_b32_e32 v52, 12, v2
	v_mov_b32_e32 v53, v23
	v_lshl_add_u64 v[2:3], s[6:7], 0, v[52:53]
	v_add_lshl_u32 v56, v4, v1, 12
	v_mov_b32_e32 v57, v23
	v_lshl_add_u64 v[54:55], v[2:3], 0, v[44:45]
	v_lshl_add_u64 v[2:3], s[6:7], 0, v[56:57]
	v_add_u32_e32 v60, 0x80000, v52
	v_mov_b32_e32 v61, v23
	v_lshl_add_u64 v[58:59], v[2:3], 0, v[44:45]
	v_lshl_add_u64 v[2:3], s[6:7], 0, v[60:61]
	v_lshl_add_u64 v[62:63], v[2:3], 0, v[44:45]
	v_readfirstlane_b32 s16, v0
	s_load_dwordx2 s[0:1], s[0:1], 0x98
	s_lshr_b32 s16, s16, 6
	s_lshl_b32 s16, s16, 10
	v_bfe_u32 v1, v0, 6, 2
	v_lshrrev_b32_e32 v80, 2, v0
	s_add_u32 m0, s16, 0
	s_nop 0
	global_load_lds_dwordx4 v[46:47], off
	s_add_u32 m0, s16, 8192
	s_nop 0
	global_load_lds_dwordx4 v[50:51], off
	s_add_u32 m0, s16, 16384
	s_nop 0
	global_load_lds_dwordx4 v[54:55], off
	s_add_u32 m0, s16, 24576
	s_nop 0
	global_load_lds_dwordx4 v[58:59], off
	s_add_u32 m0, s16, 32768
	s_nop 0
	global_load_lds_dwordx4 v[62:63], off
	s_add_u32 m0, s16, 40832
	s_nop 0
	global_load_lds_dwordx4 v[46:47], off offset:128
	s_add_u32 m0, s16, 49024
	s_nop 0
	global_load_lds_dwordx4 v[50:51], off offset:128
	s_add_u32 m0, s16, 57216
	s_nop 0
	global_load_lds_dwordx4 v[54:55], off offset:128
	s_add_u32 m0, s16, 65408
	s_nop 0
	global_load_lds_dwordx4 v[58:59], off offset:128
	s_add_u32 m0, s16, 73600
	s_nop 0
	global_load_lds_dwordx4 v[62:63], off offset:128
	s_add_u32 m0, s16, 81664
	s_nop 0
	global_load_lds_dwordx4 v[46:47], off offset:256
	s_add_u32 m0, s16, 89856
	s_nop 0
	global_load_lds_dwordx4 v[50:51], off offset:256
	s_add_u32 m0, s16, 98048
	s_nop 0
	global_load_lds_dwordx4 v[54:55], off offset:256
	s_add_u32 m0, s16, 106240
	s_nop 0
	global_load_lds_dwordx4 v[58:59], off offset:256
	s_add_u32 m0, s16, 114432
	s_nop 0
	global_load_lds_dwordx4 v[62:63], off offset:256
	s_mov_b32 s17, 0
	s_mov_b32 s18, 0xa000
	s_mov_b32 s19, 0x14000
	v_lshlrev_b32_e32 v25, 6, v0
	v_lshlrev_b32_e32 v27, 2, v0
	v_and_b32_e32 v24, 48, v0
	v_and_b32_e32 v25, 0x3c0, v25
	v_and_b32_e32 v27, 32, v27
	v_or_b32_e32 v26, v25, v24
	v_bitop3_b32 v87, v25, v27, v24 bitop3:0x36
	v_or_b32_e32 v24, v44, v60
	v_mov_b32_e32 v25, v23
	v_lshl_add_u64 v[24:25], s[6:7], 0, v[24:25]
	s_mov_b64 s[10:11], 0x100
	v_lshl_add_u64 v[70:71], v[24:25], 0, s[10:11]
	v_or_b32_e32 v24, v56, v44
	v_mov_b32_e32 v25, v23
	v_lshl_add_u64 v[24:25], s[6:7], 0, v[24:25]
	v_lshl_add_u64 v[72:73], v[24:25], 0, s[10:11]
	v_or_b32_e32 v24, v52, v44
	v_mov_b32_e32 v25, v23
	v_lshl_add_u64 v[24:25], s[6:7], 0, v[24:25]
	v_lshl_add_u64 v[74:75], v[24:25], 0, s[10:11]
	v_or_b32_e32 v24, v48, v44
	v_mov_b32_e32 v25, v23
	v_lshl_add_u64 v[24:25], s[4:5], 0, v[24:25]
	v_or_b32_e32 v22, v22, v44
	v_and_b32_e32 v81, 64, v80
	v_mul_u32_u24_e32 v86, 0x1800, v1
	v_lshl_add_u64 v[76:77], v[24:25], 0, s[10:11]
	v_lshl_add_u64 v[24:25], s[4:5], 0, v[22:23]
	v_bitop3_b32 v82, v26, v86, v27 bitop3:0xde
	v_lshlrev_b32_e32 v88, 7, v81
	v_lshl_add_u64 v[78:79], v[24:25], 0, s[10:11]
	s_mov_b64 s[4:5], 0x80
	v_mov_b32_e32 v22, v23
	v_mov_b32_e32 v24, v23
	v_mov_b32_e32 v25, v23
	v_mov_b32_e32 v50, v23
	v_mov_b32_e32 v51, v23
	v_mov_b32_e32 v52, v23
	v_mov_b32_e32 v54, v23
	v_mov_b32_e32 v55, v23
	v_mov_b32_e32 v56, v23
	v_mov_b32_e32 v58, v23
	v_mov_b32_e32 v59, v23
	v_mov_b32_e32 v60, v23
	v_mov_b32_e32 v66, v23
	v_mov_b32_e32 v67, v23
	v_mov_b32_e32 v68, v23
	v_mov_b32_e32 v69, v23
	v_mov_b32_e32 v62, v23
	v_mov_b32_e32 v63, v23
	v_mov_b32_e32 v64, v23
	v_mov_b32_e32 v65, v23
	v_mov_b32_e32 v42, v23
	v_mov_b32_e32 v43, v23
	v_mov_b32_e32 v44, v23
	v_mov_b32_e32 v46, v23
	v_mov_b32_e32 v47, v23
	v_mov_b32_e32 v48, v23
	v_mov_b32_e32 v30, v23
	v_mov_b32_e32 v31, v23
	v_mov_b32_e32 v32, v23
	v_mov_b32_e32 v33, v23
	v_mov_b32_e32 v34, v23
	v_mov_b32_e32 v35, v23
	v_mov_b32_e32 v36, v23
	v_mov_b32_e32 v37, v23
	v_mov_b32_e32 v38, v23
	v_mov_b32_e32 v39, v23
	v_mov_b32_e32 v40, v23
	v_mov_b32_e32 v41, v23
	v_mov_b32_e32 v26, v23
	v_mov_b32_e32 v27, v23
	v_mov_b32_e32 v28, v23
	v_mov_b32_e32 v29, v23
	v_add_u32_e32 v146, v87, v88
	s_waitcnt vmcnt(10) lgkmcnt(0)
	s_barrier
	ds_read_b128 v[90:93], v146
	ds_read_b128 v[106:109], v82 offset:16384
	ds_read_b128 v[110:113], v82 offset:18432
	ds_read_b128 v[114:117], v82 offset:20480
	ds_read_b128 v[94:97], v146 offset:2048
	ds_read_b128 v[98:101], v146 offset:4096
	ds_read_b128 v[102:105], v146 offset:6144
.Ldn_loop:
	v_add_u32_e32 v147, s17, v146
	v_add_u32_e32 v148, s17, v82
	ds_read_b128 v[118:121], v147 offset:1024
	ds_read_b128 v[134:137], v148 offset:17408
	ds_read_b128 v[138:141], v148 offset:19456
	ds_read_b128 v[142:145], v148 offset:21504
	ds_read_b128 v[122:125], v147 offset:3072
	ds_read_b128 v[126:129], v147 offset:5120
	ds_read_b128 v[130:133], v147 offset:7168
	s_waitcnt lgkmcnt(12)
	v_mfma_f32_16x16x32_f16 v[22:25], v[90:93], v[106:109], v[22:25]
	s_waitcnt lgkmcnt(11)
	v_mfma_f32_16x16x32_f16 v[50:53], v[90:93], v[110:113], v[50:53]
	s_waitcnt lgkmcnt(10)
	v_mfma_f32_16x16x32_f16 v[54:57], v[90:93], v[114:117], v[54:57]
	s_waitcnt lgkmcnt(9)
	v_mfma_f32_16x16x32_f16 v[58:61], v[94:97], v[106:109], v[58:61]
	v_mfma_f32_16x16x32_f16 v[66:69], v[94:97], v[110:113], v[66:69]
	v_mfma_f32_16x16x32_f16 v[62:65], v[94:97], v[114:117], v[62:65]
	s_waitcnt lgkmcnt(8)
	v_mfma_f32_16x16x32_f16 v[42:45], v[98:101], v[106:109], v[42:45]
	v_mfma_f32_16x16x32_f16 v[46:49], v[98:101], v[110:113], v[46:49]
	v_mfma_f32_16x16x32_f16 v[30:33], v[98:101], v[114:117], v[30:33]
	s_waitcnt lgkmcnt(7)
	v_mfma_f32_16x16x32_f16 v[34:37], v[102:105], v[106:109], v[34:37]
	v_mfma_f32_16x16x32_f16 v[38:41], v[102:105], v[110:113], v[38:41]
	v_mfma_f32_16x16x32_f16 v[26:29], v[102:105], v[114:117], v[26:29]
	s_waitcnt vmcnt(5) lgkmcnt(0)
	s_barrier
	v_add_u32_e32 v147, s18, v146
	v_add_u32_e32 v148, s18, v82
	ds_read_b128 v[90:93], v147
	ds_read_b128 v[106:109], v148 offset:16384
	ds_read_b128 v[110:113], v148 offset:18432
	ds_read_b128 v[114:117], v148 offset:20480
	ds_read_b128 v[94:97], v147 offset:2048
	ds_read_b128 v[98:101], v147 offset:4096
	ds_read_b128 v[102:105], v147 offset:6144
	s_add_u32 s6, s17, s16
	s_mov_b32 m0, s6
	v_lshl_add_u64 v[2:3], v[78:79], 0, s[4:5]
	global_load_lds_dwordx4 v[2:3], off
	v_mfma_f32_16x16x32_f16 v[22:25], v[118:121], v[134:137], v[22:25]
	v_mfma_f32_16x16x32_f16 v[50:53], v[118:121], v[138:141], v[50:53]
	v_mfma_f32_16x16x32_f16 v[54:57], v[118:121], v[142:145], v[54:57]
	s_add_u32 m0, s6, 8192
	v_lshl_add_u64 v[4:5], v[76:77], 0, s[4:5]
	global_load_lds_dwordx4 v[4:5], off
	v_mfma_f32_16x16x32_f16 v[58:61], v[122:125], v[134:137], v[58:61]
	v_mfma_f32_16x16x32_f16 v[66:69], v[122:125], v[138:141], v[66:69]
	v_mfma_f32_16x16x32_f16 v[62:65], v[122:125], v[142:145], v[62:65]
	s_add_u32 m0, s6, 16384
	v_lshl_add_u64 v[6:7], v[74:75], 0, s[4:5]
	global_load_lds_dwordx4 v[6:7], off
	v_mfma_f32_16x16x32_f16 v[42:45], v[126:129], v[134:137], v[42:45]
	v_mfma_f32_16x16x32_f16 v[46:49], v[126:129], v[138:141], v[46:49]
	v_mfma_f32_16x16x32_f16 v[30:33], v[126:129], v[142:145], v[30:33]
	s_add_u32 m0, s6, 24576
	v_lshl_add_u64 v[8:9], v[72:73], 0, s[4:5]
	global_load_lds_dwordx4 v[8:9], off
	v_mfma_f32_16x16x32_f16 v[34:37], v[130:133], v[134:137], v[34:37]
	s_add_u32 m0, s6, 32768
	v_lshl_add_u64 v[10:11], v[70:71], 0, s[4:5]
	global_load_lds_dwordx4 v[10:11], off
	v_mfma_f32_16x16x32_f16 v[38:41], v[130:133], v[138:141], v[38:41]
	v_mfma_f32_16x16x32_f16 v[26:29], v[130:133], v[142:145], v[26:29]
	s_add_u32 s4, s4, 0x80
	s_addc_u32 s5, s5, 0
	s_cmpk_eq_i32 s4, 0xf80
	s_mov_b32 s20, s17
	s_mov_b32 s17, s18
	s_mov_b32 s18, s19
	s_mov_b32 s19, s20
	s_cbranch_scc0 .Ldn_loop
	v_add_u32_e32 v78, v87, v88
	ds_read_b128 v[70:73], v78 offset:2048
	ds_read_b128 v[74:77], v78 offset:4096
	ds_read_b128 v[86:89], v78 offset:6144
	ds_read_b128 v[90:93], v82 offset:16384
	ds_read_b128 v[94:97], v82 offset:18432
	ds_read_b128 v[98:101], v78
	ds_read_b128 v[102:105], v82 offset:20480
	s_waitcnt lgkmcnt(1)
	v_mfma_f32_16x16x32_f16 v[22:25], v[98:101], v[90:93], v[22:25]
	v_mfma_f32_16x16x32_f16 v[50:53], v[98:101], v[94:97], v[50:53]
	s_waitcnt lgkmcnt(0)
	v_mfma_f32_16x16x32_f16 v[18:21], v[98:101], v[102:105], v[54:57]
	v_mfma_f32_16x16x32_f16 v[54:57], v[70:73], v[90:93], v[58:61]
	v_mfma_f32_16x16x32_f16 v[58:61], v[70:73], v[94:97], v[66:69]
	v_mfma_f32_16x16x32_f16 v[14:17], v[70:73], v[102:105], v[62:65]
	s_nop 2
	ds_read_b128 v[62:65], v78 offset:3072
	ds_read_b128 v[66:69], v78 offset:5120
	ds_read_b128 v[70:73], v78 offset:7168
	ds_read_b128 v[98:101], v82 offset:17408
	ds_read_b128 v[106:109], v82 offset:19456
	ds_read_b128 v[110:113], v78 offset:1024
	ds_read_b128 v[114:117], v82 offset:21504
	v_mfma_f32_16x16x32_f16 v[42:45], v[74:77], v[90:93], v[42:45]
	s_mov_b32 s3, 0xe000
	v_mfma_f32_16x16x32_f16 v[46:49], v[74:77], v[94:97], v[46:49]
	v_mfma_f32_16x16x32_f16 v[10:13], v[74:77], v[102:105], v[30:33]
	v_mfma_f32_16x16x32_f16 v[30:33], v[86:89], v[90:93], v[34:37]
	v_mfma_f32_16x16x32_f16 v[34:37], v[86:89], v[94:97], v[38:41]
	v_mfma_f32_16x16x32_f16 v[6:9], v[86:89], v[102:105], v[26:29]
	s_waitcnt lgkmcnt(1)
	v_mfma_f32_16x16x32_f16 v[22:25], v[110:113], v[98:101], v[22:25]
	v_mfma_f32_16x16x32_f16 v[26:29], v[110:113], v[106:109], v[50:53]
	s_waitcnt lgkmcnt(0)
	v_mfma_f32_16x16x32_f16 v[2:5], v[110:113], v[114:117], v[18:21]
	v_mfma_f32_16x16x32_f16 v[18:21], v[62:65], v[98:101], v[54:57]
	v_mfma_f32_16x16x32_f16 v[38:41], v[62:65], v[106:109], v[58:61]
	v_mfma_f32_16x16x32_f16 v[14:17], v[62:65], v[114:117], v[14:17]
	v_mfma_f32_16x16x32_f16 v[42:45], v[66:69], v[98:101], v[42:45]
	v_mfma_f32_16x16x32_f16 v[46:49], v[66:69], v[106:109], v[46:49]
	v_mfma_f32_16x16x32_f16 v[10:13], v[66:69], v[114:117], v[10:13]
	v_mfma_f32_16x16x32_f16 v[30:33], v[70:73], v[98:101], v[30:33]
	v_mfma_f32_16x16x32_f16 v[34:37], v[70:73], v[106:109], v[34:37]
	v_mfma_f32_16x16x32_f16 v[6:9], v[70:73], v[114:117], v[6:9]
	s_waitcnt vmcnt(0) lgkmcnt(0)
	s_barrier
	ds_read_b128 v[50:53], v78 offset:43008
	ds_read_b128 v[54:57], v78 offset:45056
	ds_read_b128 v[58:61], v78 offset:47104
	ds_read_b128 v[62:65], v82 offset:57344
	ds_read_b128 v[66:69], v82 offset:59392
	ds_read_b128 v[70:73], v78 offset:40960
	ds_read_b128 v[74:77], v82 offset:61440
	s_waitcnt lgkmcnt(1)
	v_mfma_f32_16x16x32_f16 v[22:25], v[70:73], v[62:65], v[22:25]
	v_mfma_f32_16x16x32_f16 v[26:29], v[70:73], v[66:69], v[26:29]
	s_waitcnt lgkmcnt(0)
	v_mfma_f32_16x16x32_f16 v[2:5], v[70:73], v[74:77], v[2:5]
	v_mfma_f32_16x16x32_f16 v[18:21], v[50:53], v[62:65], v[18:21]
	v_mfma_f32_16x16x32_f16 v[38:41], v[50:53], v[66:69], v[38:41]
	v_mfma_f32_16x16x32_f16 v[14:17], v[50:53], v[74:77], v[14:17]
	ds_read_b128 v[50:53], v78 offset:44032
	ds_read_b128 v[70:73], v78 offset:46080
	ds_read_b128 v[84:87], v78 offset:48128
	ds_read_b128 v[88:91], v82 offset:58368
	ds_read_b128 v[92:95], v82 offset:60416
	ds_read_b128 v[96:99], v78 offset:41984
	ds_read_b128 v[100:103], v82 offset:62464
	v_mfma_f32_16x16x32_f16 v[42:45], v[54:57], v[62:65], v[42:45]
	v_mfma_f32_16x16x32_f16 v[46:49], v[54:57], v[66:69], v[46:49]
	v_mfma_f32_16x16x32_f16 v[10:13], v[54:57], v[74:77], v[10:13]
	v_mfma_f32_16x16x32_f16 v[30:33], v[58:61], v[62:65], v[30:33]
	v_mfma_f32_16x16x32_f16 v[34:37], v[58:61], v[66:69], v[34:37]
	v_mfma_f32_16x16x32_f16 v[6:9], v[58:61], v[74:77], v[6:9]
	s_waitcnt lgkmcnt(1)
	v_mfma_f32_16x16x32_f16 v[22:25], v[96:99], v[88:91], v[22:25]
	v_mfma_f32_16x16x32_f16 v[26:29], v[96:99], v[92:95], v[26:29]
	s_waitcnt lgkmcnt(0)
	v_mfma_f32_16x16x32_f16 v[2:5], v[96:99], v[100:103], v[2:5]
	v_mfma_f32_16x16x32_f16 v[18:21], v[50:53], v[88:91], v[18:21]
	v_mfma_f32_16x16x32_f16 v[38:41], v[50:53], v[92:95], v[38:41]
	v_mfma_f32_16x16x32_f16 v[14:17], v[50:53], v[100:103], v[14:17]
	v_mfma_f32_16x16x32_f16 v[42:45], v[70:73], v[88:91], v[42:45]
	v_mfma_f32_16x16x32_f16 v[46:49], v[70:73], v[92:95], v[46:49]
	v_mfma_f32_16x16x32_f16 v[10:13], v[70:73], v[100:103], v[10:13]
	v_mfma_f32_16x16x32_f16 v[30:33], v[84:87], v[88:91], v[30:33]
	v_mfma_f32_16x16x32_f16 v[34:37], v[84:87], v[92:95], v[34:37]
	v_mfma_f32_16x16x32_f16 v[6:9], v[84:87], v[100:103], v[6:9]
	v_and_or_b32 v50, v80, 12, v81
	v_add_u32_e32 v50, s2, v50
	v_mul_u32_u24_e32 v1, 48, v1
	v_and_or_b32 v52, v0, 15, v1
	v_mul_u32_u24_e32 v0, 0xc00, v50
	v_mov_b32_e32 v1, 0
	v_lshl_add_u64 v[50:51], s[0:1], 0, v[0:1]
	v_add_lshl_u32 v0, v52, s8, 2
	v_lshl_add_u64 v[0:1], v[50:51], 0, v[0:1]
	s_mov_b64 s[0:1], 0x1800
	s_barrier
	global_store_dword v[0:1], v22, off
	global_store_dword v[0:1], v26, off offset:64
	global_store_dword v[0:1], v2, off offset:128
	global_store_dword v[0:1], v23, off offset:3072
	global_store_dword v[0:1], v27, off offset:3136
	global_store_dword v[0:1], v3, off offset:3200
	v_lshl_add_u64 v[2:3], v[0:1], 0, s[0:1]
	s_movk_i32 s0, 0x1000
	v_add_co_u32_e32 v22, vcc, s0, v0
	s_mov_b64 s[0:1], 0x2400
	s_nop 0
	v_addc_co_u32_e32 v23, vcc, 0, v1, vcc
	global_store_dword v[22:23], v24, off offset:2048
	global_store_dword v[2:3], v28, off offset:64
	global_store_dword v[2:3], v4, off offset:128
	v_lshl_add_u64 v[2:3], v[0:1], 0, s[0:1]
	s_movk_i32 s0, 0x2000
	v_add_co_u32_e32 v22, vcc, s0, v0
	s_mov_b64 s[0:1], 0xc000
	s_nop 0
	v_addc_co_u32_e32 v23, vcc, 0, v1, vcc
	global_store_dword v[22:23], v25, off offset:1024
	global_store_dword v[2:3], v29, off offset:64
	global_store_dword v[2:3], v5, off offset:128
	v_lshl_add_u64 v[2:3], v[0:1], 0, s[0:1]
	s_mov_b32 s0, 0xc000
	v_add_co_u32_e32 v4, vcc, s0, v0
	s_mov_b64 s[0:1], 0xcc00
	s_nop 0
	v_addc_co_u32_e32 v5, vcc, 0, v1, vcc
	global_store_dword v[4:5], v18, off
	global_store_dword v[2:3], v38, off offset:64
	global_store_dword v[2:3], v14, off offset:128
	v_lshl_add_u64 v[2:3], v[0:1], 0, s[0:1]
	s_mov_b64 s[0:1], 0xd800
	global_store_dword v[4:5], v19, off offset:3072
	global_store_dword v[2:3], v39, off offset:64
	global_store_dword v[2:3], v15, off offset:128
	v_lshl_add_u64 v[2:3], v[0:1], 0, s[0:1]
	s_mov_b32 s0, 0xd000
	v_add_co_u32_e32 v4, vcc, s0, v0
	s_mov_b64 s[0:1], 0xe400
	s_nop 0
	v_addc_co_u32_e32 v5, vcc, 0, v1, vcc
	global_store_dword v[4:5], v20, off offset:2048
	global_store_dword v[2:3], v40, off offset:64
	global_store_dword v[2:3], v16, off offset:128
	v_add_co_u32_e32 v4, vcc, s3, v0
	v_lshl_add_u64 v[2:3], v[0:1], 0, s[0:1]
	s_nop 0
	v_addc_co_u32_e32 v5, vcc, 0, v1, vcc
	s_mov_b64 s[0:1], 0x18000
	global_store_dword v[4:5], v21, off offset:1024
	global_store_dword v[2:3], v41, off offset:64
	global_store_dword v[2:3], v17, off offset:128
	v_lshl_add_u64 v[2:3], v[0:1], 0, s[0:1]
	s_mov_b32 s0, 0x18000
	v_add_co_u32_e32 v4, vcc, s0, v0
	s_mov_b64 s[0:1], 0x18c00
	s_nop 0
	v_addc_co_u32_e32 v5, vcc, 0, v1, vcc
	global_store_dword v[4:5], v42, off
	global_store_dword v[2:3], v46, off offset:64
	global_store_dword v[2:3], v10, off offset:128
	v_lshl_add_u64 v[2:3], v[0:1], 0, s[0:1]
	s_mov_b64 s[0:1], 0x19800
	global_store_dword v[4:5], v43, off offset:3072
	global_store_dword v[2:3], v47, off offset:64
	global_store_dword v[2:3], v11, off offset:128
	v_lshl_add_u64 v[2:3], v[0:1], 0, s[0:1]
	s_mov_b32 s0, 0x19000
	v_add_co_u32_e32 v4, vcc, s0, v0
	s_mov_b64 s[0:1], 0x1a400
	s_nop 0
	v_addc_co_u32_e32 v5, vcc, 0, v1, vcc
	global_store_dword v[4:5], v44, off offset:2048
	global_store_dword v[2:3], v48, off offset:64
	global_store_dword v[2:3], v12, off offset:128
	v_lshl_add_u64 v[2:3], v[0:1], 0, s[0:1]
	s_mov_b32 s0, 0x1a000
	v_add_co_u32_e32 v4, vcc, s0, v0
	s_mov_b64 s[0:1], 0x24000
	s_nop 0
	v_addc_co_u32_e32 v5, vcc, 0, v1, vcc
	global_store_dword v[4:5], v45, off offset:1024
	global_store_dword v[2:3], v49, off offset:64
	global_store_dword v[2:3], v13, off offset:128
	v_lshl_add_u64 v[2:3], v[0:1], 0, s[0:1]
	s_mov_b32 s0, 0x24000
	v_add_co_u32_e32 v4, vcc, s0, v0
	s_mov_b64 s[0:1], 0x24c00
	s_nop 0
	v_addc_co_u32_e32 v5, vcc, 0, v1, vcc
	global_store_dword v[4:5], v30, off
	global_store_dword v[2:3], v34, off offset:64
	global_store_dword v[2:3], v6, off offset:128
	v_lshl_add_u64 v[2:3], v[0:1], 0, s[0:1]
	s_mov_b64 s[0:1], 0x25800
	global_store_dword v[4:5], v31, off offset:3072
	global_store_dword v[2:3], v35, off offset:64
	global_store_dword v[2:3], v7, off offset:128
	v_lshl_add_u64 v[2:3], v[0:1], 0, s[0:1]
	s_mov_b32 s0, 0x25000
	v_add_co_u32_e32 v4, vcc, s0, v0
	s_mov_b64 s[0:1], 0x26400
	s_nop 0
	v_addc_co_u32_e32 v5, vcc, 0, v1, vcc
	global_store_dword v[4:5], v32, off offset:2048
	global_store_dword v[2:3], v36, off offset:64
	global_store_dword v[2:3], v8, off offset:128
	v_lshl_add_u64 v[2:3], v[0:1], 0, s[0:1]
	v_add_co_u32_e32 v0, vcc, 0x26000, v0
	s_nop 1
	v_addc_co_u32_e32 v1, vcc, 0, v1, vcc
	global_store_dword v[0:1], v33, off offset:1024
	global_store_dword v[2:3], v37, off offset:64
	global_store_dword v[2:3], v9, off offset:128

	.amdhsa_kernel _Z11gemm_kernelILi128ELi192ELi1EEv8GemmArgs
		.amdhsa_group_segment_fixed_size 122880
		.amdhsa_private_segment_fixed_size 0
		.amdhsa_kernarg_size 160
		.amdhsa_user_sgpr_count 2
		.amdhsa_user_sgpr_dispatch_ptr 0
		.amdhsa_user_sgpr_queue_ptr 0
		.amdhsa_user_sgpr_kernarg_segment_ptr 1
		.amdhsa_user_sgpr_dispatch_id 0
		.amdhsa_user_sgpr_kernarg_preload_length 0
		.amdhsa_user_sgpr_kernarg_preload_offset 0
		.amdhsa_user_sgpr_private_segment_size 0
		.amdhsa_uses_dynamic_stack 0
		.amdhsa_enable_private_segment 0
		.amdhsa_system_sgpr_workgroup_id_x 1
		.amdhsa_system_sgpr_workgroup_id_y 0
		.amdhsa_system_sgpr_workgroup_id_z 0
		.amdhsa_system_sgpr_workgroup_info 0
		.amdhsa_system_vgpr_workitem_id 0
		.amdhsa_next_free_vgpr 149
		.amdhsa_next_free_sgpr 96
		.amdhsa_accum_offset 152
		.amdhsa_reserve_vcc 1
		.amdhsa_float_round_mode_32 0
		.amdhsa_float_round_mode_16_64 0
		.amdhsa_float_denorm_mode_32 3
		.amdhsa_float_denorm_mode_16_64 3
		.amdhsa_dx10_clamp 1
		.amdhsa_ieee_mode 1
		.amdhsa_fp16_overflow 0
		.amdhsa_tg_split 0
		.amdhsa_exception_fp_ieee_invalid_op 0
		.amdhsa_exception_fp_denorm_src 0
		.amdhsa_exception_fp_ieee_div_zero 0
		.amdhsa_exception_fp_ieee_overflow 0
		.amdhsa_exception_fp_ieee_underflow 0
		.amdhsa_exception_fp_ieee_inexact 0
		.amdhsa_exception_int_div_zero 0
	.end_amdhsa_kernel

amdhsa.kernels:
  - .agpr_count:     0
    .args:
      - .actual_access:  read_only
        .address_space:  global
        .offset:         0
        .size:           8
        .value_kind:     global_buffer
      - .actual_access:  read_only
        .address_space:  global
        .offset:         8
        .size:           8
        .value_kind:     global_buffer
      - .actual_access:  write_only
        .address_space:  global
        .offset:         16
        .size:           8
        .value_kind:     global_buffer
      - .actual_access:  write_only
        .address_space:  global
        .offset:         24
        .size:           8
        .value_kind:     global_buffer
      - .actual_access:  write_only
        .address_space:  global
        .offset:         32
        .size:           8
        .value_kind:     global_buffer
      - .actual_access:  read_only
        .address_space:  global
        .offset:         40
        .size:           8
        .value_kind:     global_buffer
    .group_segment_fixed_size: 0
    .kernarg_segment_align: 8
    .kernarg_segment_size: 48
    .language:       OpenCL C
    .language_version:
      - 2
      - 0
    .max_flat_workgroup_size: 256
    .name:           _Z11gate_kernelPKfS0_PDF16_PiPfS3_
    .private_segment_fixed_size: 0
    .sgpr_count:     26
    .sgpr_spill_count: 0
    .symbol:         _Z11gate_kernelPKfS0_PDF16_PiPfS3_.kd
    .uniform_work_group_size: 1
    .uses_dynamic_stack: false
    .vgpr_count:     113
    .vgpr_spill_count: 0
    .wavefront_size: 64
  - .agpr_count:     0
    .args:
      - .offset:         0
        .size:           160
        .value_kind:     by_value
    .group_segment_fixed_size: 149540
    .kernarg_segment_align: 8
    .kernarg_segment_size: 160
    .language:       OpenCL C
    .language_version:
      - 2
      - 0
    .max_flat_workgroup_size: 512
    .name:           _Z9up_kernel8GemmArgs
    .private_segment_fixed_size: 0
    .sgpr_count:     82
    .sgpr_spill_count: 0
    .symbol:         _Z9up_kernel8GemmArgs.kd
    .uniform_work_group_size: 1
    .uses_dynamic_stack: false
    .vgpr_count:     256
    .vgpr_spill_count: 0
    .wavefront_size: 64
  - .agpr_count:     0
    .args:
      - .actual_access:  read_only
        .address_space:  global
        .offset:         0
        .size:           8
        .value_kind:     global_buffer
      - .actual_access:  read_only
        .address_space:  global
        .offset:         8
        .size:           8
        .value_kind:     global_buffer
      - .actual_access:  read_only
        .address_space:  global
        .offset:         16
        .size:           8
        .value_kind:     global_buffer
      - .actual_access:  write_only
        .address_space:  global
        .offset:         24
        .size:           8
        .value_kind:     global_buffer
    .group_segment_fixed_size: 0
    .kernarg_segment_align: 8
    .kernarg_segment_size: 32
    .language:       OpenCL C
    .language_version:
      - 2
      - 0
    .max_flat_workgroup_size: 256
    .name:           _Z14combine_kernelPKfPKiS0_Pf
    .private_segment_fixed_size: 0
    .sgpr_count:     18
    .sgpr_spill_count: 0
    .symbol:         _Z14combine_kernelPKfPKiS0_Pf.kd
    .uniform_work_group_size: 1
    .uses_dynamic_stack: false
    .vgpr_count:     20
    .vgpr_spill_count: 0
    .wavefront_size: 64
  - .agpr_count:     0
    .args:
      - .offset:         0
        .size:           160
        .value_kind:     by_value
    .group_segment_fixed_size: 122880
    .kernarg_segment_align: 8
    .kernarg_segment_size: 160
    .language:       OpenCL C
    .language_version:
      - 2
      - 0
    .max_flat_workgroup_size: 512
    .name:           _Z11gemm_kernelILi128ELi192ELi1EEv8GemmArgs
    .private_segment_fixed_size: 0
    .sgpr_count:     18
    .sgpr_spill_count: 0
    .symbol:         _Z11gemm_kernelILi128ELi192ELi1EEv8GemmArgs.kd
    .uniform_work_group_size: 1
    .uses_dynamic_stack: false
    .vgpr_count:     149
    .vgpr_spill_count: 0
    .wavefront_size: 64
